# attention phase schedule: mid conversion quota of rank<8 workgroups 18 -> 0 (they go straight to gate-projection GEMM units after their now-short attention unit; conversions overlap on the other half)
# speedup vs baseline: 1.0650x; 1.0328x over previous
.LBB0_724:
	s_cmpk_lt_i32 s8, 0x80
	s_cselect_b32 s6, 0, 0
	s_and_b64 s[2:3], s[4:5], exec
	s_cselect_b32 s16, s6, 4
	s_cmp_lg_u32 s16, 0
	v_mov_b32_e32 v206, v205
	v_mov_b32_e32 v207, v213
	v_mov_b32_e32 v213, v209
	v_mov_b32_e32 v209, v211
	v_or_b32_e32 v211, 0x60, v1
	s_waitcnt lgkmcnt(0)
	s_barrier
	s_cbranch_scc0 .LBB0_931
	s_and_saveexec_b64 s[2:3], s[0:1]
	v_readlane_b32 s36, v254, 38
	v_readlane_b32 s46, v254, 48
	v_readlane_b32 s47, v254, 49
	v_readlane_b32 s50, v254, 52
	v_readlane_b32 s51, v254, 53
	v_readlane_b32 s37, v254, 39
	v_readlane_b32 s38, v254, 40
	v_readlane_b32 s39, v254, 41
	v_readlane_b32 s40, v254, 42
	v_readlane_b32 s41, v254, 43
	v_readlane_b32 s42, v254, 44
	v_readlane_b32 s43, v254, 45
	v_readlane_b32 s44, v254, 46
	v_readlane_b32 s45, v254, 47
	v_readlane_b32 s48, v254, 50
	v_readlane_b32 s49, v254, 51
	s_cbranch_execz .LBB0_729
	s_mov_b64 s[6:7], exec
	s_waitcnt vmcnt(15)
	v_mbcnt_lo_u32_b32 v2, s6, 0
	v_mbcnt_hi_u32_b32 v2, s7, v2
	v_cmp_eq_u32_e32 vcc, 0, v2
	s_and_saveexec_b64 s[4:5], vcc
	s_cbranch_execz .LBB0_728
	s_bcnt1_i32_b64 s6, s[6:7]
	v_mov_b32_e32 v3, 0
	v_mov_b32_e32 v4, s6
	global_atomic_add v3, v3, v4, s[50:51] offset:1280 sc0

.LBB0_2292:
	s_cmpk_lt_i32 s8, 0x80
	s_cselect_b32 s6, 0, 0
	s_and_b64 s[2:3], s[4:5], exec
	s_cselect_b32 s33, s6, 4
	s_cmp_lg_u32 s33, 0
	v_mov_b32_e32 v206, v205
	v_mov_b32_e32 v207, v213
	v_mov_b32_e32 v213, v209
	v_mov_b32_e32 v209, v211
	v_or_b32_e32 v211, 0x60, v1
	s_waitcnt lgkmcnt(0)
	s_barrier
	s_cbranch_scc0 .LBB0_2499
	s_and_saveexec_b64 s[2:3], s[0:1]
	s_cbranch_execz .LBB0_2297
	s_mov_b64 s[6:7], exec
	s_waitcnt vmcnt(15)
	v_mbcnt_lo_u32_b32 v2, s6, 0
	v_mbcnt_hi_u32_b32 v2, s7, v2
	v_cmp_eq_u32_e32 vcc, 0, v2
	s_and_saveexec_b64 s[4:5], vcc
	s_cbranch_execz .LBB0_2296
	s_bcnt1_i32_b64 s6, s[6:7]
	v_mov_b32_e32 v3, 0
	v_mov_b32_e32 v4, s6
	global_atomic_add v3, v3, v4, s[94:95] offset:1536 sc0
